# phase-0 one-time stagger: waves 4-7 sleep ~16k cycles at phase-0 start to de-phase load-wait and LDS/VALU work across the CU's waves
# baseline (speedup 1.0000x reference)
.LBB0_7:
	s_load_dwordx16 s[64:79], s[0:1], 0x50
	s_load_dwordx16 s[36:51], s[0:1], 0x90
	s_lshl_b32 s94, s97, 3
	s_cmp_lt_i32 s90, 1
	s_cselect_b64 s[0:1], -1, 0
	s_cmp_gt_i32 s91, 0
	s_waitcnt lgkmcnt(0)
	v_writelane_b32 v239, s36, 7
	s_cselect_b64 s[2:3], -1, 0
	s_lshl_b32 s83, s96, 3
	v_writelane_b32 v239, s37, 8
	v_writelane_b32 v239, s38, 9
	v_writelane_b32 v239, s39, 10
	v_writelane_b32 v239, s40, 11
	v_writelane_b32 v239, s41, 12
	v_writelane_b32 v239, s42, 13
	v_writelane_b32 v239, s43, 14
	v_writelane_b32 v239, s44, 15
	v_writelane_b32 v239, s45, 16
	v_writelane_b32 v239, s46, 17
	v_writelane_b32 v239, s47, 18
	v_writelane_b32 v239, s48, 19
	v_writelane_b32 v239, s49, 20
	v_writelane_b32 v239, s50, 21
	v_writelane_b32 v239, s51, 22
	v_writelane_b32 v239, s83, 23
	v_writelane_b32 v239, s88, 24
	s_and_b64 s[0:1], s[0:1], s[2:3]
	s_andn2_b64 vcc, exec, s[0:1]
	v_writelane_b32 v239, s89, 25
	v_writelane_b32 v239, s90, 26
	v_writelane_b32 v239, s91, 27
	s_cbranch_vccnz .LBB0_175
	v_mov_b32_e32 v1, v0
	s_lshl_b32 s39, s96, 9
	v_readfirstlane_b32 s0, v1
	s_ashr_i32 s0, s0, 6
	s_cmp_lt_u32 s0, 4
	s_cbranch_scc1 .Lp0_nostagger
	s_sleep 127
	s_sleep 127
.Lp0_nostagger:
	s_lshl_b32 s52, s97, 9
	s_add_i32 s62, s0, s83
	s_mov_b32 s2, s94
	s_cmpk_lt_i32 s62, 0x7600
	v_writelane_b32 v239, s2, 28
	s_nop 1
	v_writelane_b32 v239, s3, 29
	s_cbranch_scc0 .LBB0_102
	s_mul_i32 s1, s0, 0x4100
	v_writelane_b32 v239, s33, 30
	s_add_i32 s41, s1, 0
	v_writelane_b32 v239, s1, 31
	s_add_u32 s1, s88, 0xd900000
	v_writelane_b32 v239, s1, 33
	s_addc_u32 s1, s89, 0
	v_writelane_b32 v239, s1, 35
	s_add_u32 s1, s88, 0xb900000
	v_writelane_b32 v239, s1, 37
	s_addc_u32 s1, s89, 0
	v_writelane_b32 v239, s1, 39
	s_add_u32 s1, s88, 0x7900000
	v_writelane_b32 v239, s1, 40
	s_addc_u32 s1, s89, 0
	s_add_u32 s95, s88, 0x100000
	v_writelane_b32 v239, s1, 42
	s_addc_u32 s44, s89, 0
	s_lshl_b32 s1, s0, 6
	s_add_i32 s3, s39, s1
	s_lshl_b32 s1, s96, 4
	s_lshl_b32 s0, s0, 1
	s_add_i32 s9, s1, s0
	s_lshl_b32 s0, s62, 2
	v_and_b32_e32 v136, 63, v1
	s_mov_b32 s92, 0
	v_writelane_b32 v239, s96, 44
	s_lshl_b32 s96, s97, 4
	s_add_i32 s36, s0, 0xffff4400
	s_lshl_b32 s2, s97, 5
	s_mov_b64 s[0:1], 0
	s_mov_b32 s37, s3
	s_mov_b32 s33, s62
	s_mov_b64 s[4:5], 0
	s_mov_b32 s91, 0
	s_mov_b32 s6, 0
	s_mov_b32 s8, 0
	s_mov_b32 s60, 0
	s_mov_b32 s61, 0
	s_mov_b32 s40, s95
